# v52 + GQA QK^T: one counted LDS wait per fragment round (two back-to-back MFMAs) instead of one per MFMA; finish-softmax VALU in 8 gaps
# baseline (speedup 1.0000x reference)
.LBB0_881:
	ds_read_b128 v[96:99], v216 offset:49152
	ds_read_b128 v[100:103], v216 offset:57344
	ds_read_b128 v[178:181], v218 offset:49152
	ds_read_b128 v[182:185], v218 offset:57344
	ds_read_b128 v[240:243], v219 offset:49152
	ds_read_b128 v[244:247], v219 offset:57344
	v_add_f32_e32 v88, v64, v65
	v_add_f32_e32 v89, v72, v73
	v_add_f32_e32 v90, v80, v81
	v_add_f32_e32 v91, v194, v195
	v_add_f32_e32 v88, v66, v88
	v_add_f32_e32 v89, v74, v89
	v_add_f32_e32 v90, v82, v90
	s_waitcnt lgkmcnt(4)
	v_mfma_f32_32x32x16_bf16 v[112:127], v[96:99], v[138:141], 0
	v_mfma_f32_32x32x16_bf16 v[96:111], v[100:103], v[138:141], 0
	v_add_f32_e32 v91, v196, v91
	v_add_f32_e32 v88, v67, v88
	v_add_f32_e32 v89, v75, v89
	v_add_f32_e32 v90, v83, v90
	v_add_f32_e32 v91, v197, v91
	v_add_f32_e32 v88, v68, v88
	v_add_f32_e32 v89, v76, v89
	s_waitcnt lgkmcnt(2)
	v_mfma_f32_32x32x16_bf16 v[112:127], v[178:181], v[154:157], v[112:127]
	v_mfma_f32_32x32x16_bf16 v[96:111], v[182:185], v[154:157], v[96:111]
	ds_read_b128 v[178:181], v220 offset:49152
	ds_read_b128 v[182:185], v220 offset:57344
	v_add_f32_e32 v90, v84, v90
	v_add_f32_e32 v91, v92, v91
	v_add_f32_e32 v88, v69, v88
	v_add_f32_e32 v89, v77, v89
	v_add_f32_e32 v90, v85, v90
	v_add_f32_e32 v91, v93, v91
	v_add_f32_e32 v88, v70, v88
	s_waitcnt lgkmcnt(2)
	v_mfma_f32_32x32x16_bf16 v[112:127], v[240:243], v[158:161], v[112:127]
	v_mfma_f32_32x32x16_bf16 v[96:111], v[244:247], v[158:161], v[96:111]
	ds_read_b128 v[240:243], v221 offset:49152
	ds_read_b128 v[244:247], v221 offset:57344
	v_add_f32_e32 v89, v78, v89
	v_add_f32_e32 v90, v86, v90
	v_add_f32_e32 v91, v94, v91
	v_add_f32_e32 v88, v71, v88
	v_add_f32_e32 v89, v79, v89
	v_add_f32_e32 v90, v87, v90
	v_add_f32_e32 v91, v95, v91
	s_waitcnt lgkmcnt(2)
	v_mfma_f32_32x32x16_bf16 v[112:127], v[178:181], v[150:153], v[112:127]
	v_mfma_f32_32x32x16_bf16 v[96:111], v[182:185], v[150:153], v[96:111]
	ds_read_b128 v[178:181], v222 offset:49152
	ds_read_b128 v[182:185], v222 offset:57344
	v_add_f32_e32 v88, v89, v88
	v_add_f32_e32 v89, v91, v90
	v_add_f32_e32 v227, v88, v89
	v_mov_b32_e32 v228, v227
	v_cvt_pk_bf16_f32 v88, v64, v65
	v_cvt_pk_bf16_f32 v89, v66, v67
	v_cvt_pk_bf16_f32 v90, v68, v69
	v_cvt_pk_bf16_f32 v91, v70, v71
	s_waitcnt lgkmcnt(2)
	v_mfma_f32_32x32x16_bf16 v[112:127], v[240:243], v[146:149], v[112:127]
	v_mfma_f32_32x32x16_bf16 v[96:111], v[244:247], v[146:149], v[96:111]
	ds_read_b128 v[240:243], v224 offset:49152
	ds_read_b128 v[244:247], v224 offset:57344
	v_permlane32_swap_b32_e32 v227, v228
	v_cvt_pk_bf16_f32 v72, v72, v73
	v_cvt_pk_bf16_f32 v73, v74, v75
	v_cvt_pk_bf16_f32 v74, v76, v77
	v_cvt_pk_bf16_f32 v75, v78, v79
	s_waitcnt lgkmcnt(2)
	v_mfma_f32_32x32x16_bf16 v[112:127], v[178:181], v[142:145], v[112:127]
	v_mfma_f32_32x32x16_bf16 v[96:111], v[182:185], v[142:145], v[96:111]
	ds_read_b128 v[178:181], v223 offset:49152
	ds_read_b128 v[182:185], v223 offset:57344
	v_cvt_pk_bf16_f32 v64, v80, v81
	v_cvt_pk_bf16_f32 v65, v82, v83
	v_cvt_pk_bf16_f32 v66, v84, v85
	v_cvt_pk_bf16_f32 v67, v86, v87
	v_cvt_pk_bf16_f32 v68, v194, v195
	v_cvt_pk_bf16_f32 v69, v196, v197
	v_cvt_pk_bf16_f32 v70, v92, v93
	s_waitcnt lgkmcnt(2)
	v_mfma_f32_32x32x16_bf16 v[112:127], v[240:243], v[134:137], v[112:127]
	v_mfma_f32_32x32x16_bf16 v[96:111], v[244:247], v[134:137], v[96:111]
	v_cvt_pk_bf16_f32 v71, v94, v95
	s_waitcnt lgkmcnt(0)
	v_mfma_f32_32x32x16_bf16 v[112:127], v[178:181], v[130:133], v[112:127]
	v_mfma_f32_32x32x16_bf16 v[96:111], v[182:185], v[130:133], v[96:111]
	s_add_i32 s2, s39, -1
	s_mul_i32 s2, s2, s62
	s_lshl_b32 s72, s2, 6
	s_lshl_b64 s[2:3], s[72:73], 1
	s_add_u32 s12, s10, s2
	s_addc_u32 s13, s11, s3
	s_add_u32 s2, s8, s2
	s_addc_u32 s3, s9, s3
	global_load_dwordx4 v[178:181], v128, s[12:13]
	global_load_dwordx4 v[182:185], v198, s[12:13]
	global_load_dwordx4 v[186:189], v128, s[2:3]
	global_load_dwordx4 v[190:193], v198, s[2:3]
	ds_read_b64_tr_b16 v[76:77], v209 offset:0
	ds_read_b64_tr_b16 v[78:79], v209 offset:0x800
	ds_read_b64_tr_b16 v[80:81], v209 offset:0x1000
	ds_read_b64_tr_b16 v[82:83], v209 offset:0x1800
	ds_read_b64_tr_b16 v[84:85], v209 offset:0x2000
	ds_read_b64_tr_b16 v[86:87], v209 offset:0x2800
	ds_read_b64_tr_b16 v[92:93], v209 offset:0x3000
	ds_read_b64_tr_b16 v[94:95], v209 offset:0x3800
	s_waitcnt lgkmcnt(0)
	s_nop 0
	v_mfma_f32_32x32x16_bf16 v[0:15], v[76:79], v[88:91], v[0:15]
	v_mfma_f32_32x32x16_bf16 v[0:15], v[80:83], v[72:75], v[0:15]
	v_mfma_f32_32x32x16_bf16 v[0:15], v[84:87], v[64:67], v[0:15]
	ds_read_b64_tr_b16 v[76:77], v209 offset:0x200
	ds_read_b64_tr_b16 v[78:79], v209 offset:0xa00
	ds_read_b64_tr_b16 v[80:81], v209 offset:0x1200
	v_mfma_f32_32x32x16_bf16 v[0:15], v[92:95], v[68:71], v[0:15]
	ds_read_b64_tr_b16 v[82:83], v209 offset:0x1a00
	ds_read_b64_tr_b16 v[84:85], v209 offset:0x2200
	ds_read_b64_tr_b16 v[86:87], v209 offset:0x2a00
	ds_read_b64_tr_b16 v[92:93], v209 offset:0x3200
	ds_read_b64_tr_b16 v[94:95], v209 offset:0x3a00
	s_waitcnt lgkmcnt(0)
	v_mfma_f32_32x32x16_bf16 v[48:63], v[76:79], v[88:91], v[48:63]
	v_mfma_f32_32x32x16_bf16 v[48:63], v[80:83], v[72:75], v[48:63]
	v_mfma_f32_32x32x16_bf16 v[48:63], v[84:87], v[64:67], v[48:63]
	ds_read_b64_tr_b16 v[76:77], v209 offset:0x400
	ds_read_b64_tr_b16 v[78:79], v209 offset:0xc00
	ds_read_b64_tr_b16 v[80:81], v209 offset:0x1400
	ds_read_b64_tr_b16 v[82:83], v209 offset:0x1c00
	v_mfma_f32_32x32x16_bf16 v[48:63], v[92:95], v[68:71], v[48:63]
	ds_read_b64_tr_b16 v[84:85], v209 offset:0x2400
	ds_read_b64_tr_b16 v[86:87], v209 offset:0x2c00
	ds_read_b64_tr_b16 v[92:93], v209 offset:0x3400
	ds_read_b64_tr_b16 v[94:95], v209 offset:0x3c00
	s_waitcnt lgkmcnt(0)
	v_mfma_f32_32x32x16_bf16 v[32:47], v[76:79], v[88:91], v[32:47]
	ds_read_b64_tr_b16 v[76:77], v209 offset:0x600
	ds_read_b64_tr_b16 v[78:79], v209 offset:0xe00
	v_exp_f32_e32 v234, v104
	v_exp_f32_e32 v235, v105
	v_exp_f32_e32 v236, v106
	v_exp_f32_e32 v237, v107
	v_exp_f32_e32 v238, v108
	v_exp_f32_e32 v239, v109
	v_exp_f32_e32 v231, v110
	v_exp_f32_e32 v249, v111
	v_mfma_f32_32x32x16_bf16 v[32:47], v[80:83], v[72:75], v[32:47]
	v_exp_f32_e32 v80, v112
	v_exp_f32_e32 v81, v113
	v_exp_f32_e32 v82, v114
	v_exp_f32_e32 v83, v115
	v_mfma_f32_32x32x16_bf16 v[32:47], v[84:87], v[64:67], v[32:47]
	v_exp_f32_e32 v84, v116
	v_exp_f32_e32 v85, v117
	v_exp_f32_e32 v86, v118
	v_exp_f32_e32 v87, v119
	v_exp_f32_e32 v112, v96
	v_exp_f32_e32 v113, v97
	v_exp_f32_e32 v114, v98
	v_exp_f32_e32 v115, v99
	v_exp_f32_e32 v116, v100
	v_exp_f32_e32 v117, v101
	v_exp_f32_e32 v118, v102
	v_exp_f32_e32 v119, v103
	v_mfma_f32_32x32x16_bf16 v[32:47], v[92:95], v[68:71], v[32:47]
	ds_read_b64_tr_b16 v[92:93], v209 offset:0x1600
	ds_read_b64_tr_b16 v[94:95], v209 offset:0x1e00
	ds_read_b64_tr_b16 v[96:97], v209 offset:0x2600
	ds_read_b64_tr_b16 v[98:99], v209 offset:0x2e00
	ds_read_b64_tr_b16 v[100:101], v209 offset:0x3600
	ds_read_b64_tr_b16 v[102:103], v209 offset:0x3e00
	s_waitcnt lgkmcnt(0)
	v_mfma_f32_32x32x16_bf16 v[16:31], v[76:79], v[88:91], v[16:31]
	v_exp_f32_e32 v88, v120
	v_exp_f32_e32 v89, v121
	v_exp_f32_e32 v90, v122
	v_exp_f32_e32 v91, v123
	v_mfma_f32_32x32x16_bf16 v[16:31], v[92:95], v[72:75], v[16:31]
	v_exp_f32_e32 v92, v124
	v_exp_f32_e32 v93, v125
	v_exp_f32_e32 v94, v126
	v_exp_f32_e32 v95, v127
	s_barrier
	v_mfma_f32_32x32x16_bf16 v[16:31], v[96:99], v[64:67], v[16:31]
	s_waitcnt vmcnt(4)
	s_waitcnt vmcnt(7)
	ds_write_b128 v212, v[162:165]
	s_waitcnt vmcnt(6)
	ds_write_b128 v213, v[166:169]
	s_waitcnt vmcnt(5)
	ds_write_b128 v214, v[170:173] offset:32768
	s_waitcnt vmcnt(4)
	ds_write_b128 v215, v[174:177] offset:32768
	v_mfma_f32_32x32x16_bf16 v[16:31], v[100:103], v[68:71], v[16:31]
.LBB0_883:
	s_waitcnt lgkmcnt(0)
	s_barrier
	ds_read_b128 v[64:67], v216 offset:32768
	ds_read_b128 v[68:71], v216 offset:40960
	ds_read_b128 v[162:165], v218 offset:32768
	ds_read_b128 v[166:169], v218 offset:40960
	ds_read_b128 v[240:243], v219 offset:32768
	ds_read_b128 v[244:247], v219 offset:40960
	v_add_f32_e32 v120, v80, v81
	v_add_f32_e32 v121, v88, v89
	v_add_f32_e32 v122, v112, v113
	v_add_f32_e32 v123, v234, v235
	v_add_f32_e32 v120, v82, v120
	v_add_f32_e32 v121, v90, v121
	v_add_f32_e32 v122, v114, v122
	s_waitcnt lgkmcnt(4)
	v_mfma_f32_32x32x16_bf16 v[96:111], v[64:67], v[138:141], 0
	v_mfma_f32_32x32x16_bf16 v[64:79], v[68:71], v[138:141], 0
	v_add_f32_e32 v123, v236, v123
	v_add_f32_e32 v120, v83, v120
	v_add_f32_e32 v121, v91, v121
	v_add_f32_e32 v122, v115, v122
	v_add_f32_e32 v123, v237, v123
	v_add_f32_e32 v120, v84, v120
	v_add_f32_e32 v121, v92, v121
	s_waitcnt lgkmcnt(2)
	v_mfma_f32_32x32x16_bf16 v[96:111], v[162:165], v[154:157], v[96:111]
	v_mfma_f32_32x32x16_bf16 v[64:79], v[166:169], v[154:157], v[64:79]
	ds_read_b128 v[162:165], v220 offset:32768
	ds_read_b128 v[166:169], v220 offset:40960
	v_add_f32_e32 v122, v116, v122
	v_add_f32_e32 v123, v238, v123
	v_add_f32_e32 v120, v85, v120
	v_add_f32_e32 v121, v93, v121
	v_add_f32_e32 v122, v117, v122
	v_add_f32_e32 v123, v239, v123
	v_add_f32_e32 v120, v86, v120
	s_waitcnt lgkmcnt(2)
	v_mfma_f32_32x32x16_bf16 v[96:111], v[240:243], v[158:161], v[96:111]
	v_mfma_f32_32x32x16_bf16 v[64:79], v[244:247], v[158:161], v[64:79]
	ds_read_b128 v[240:243], v221 offset:32768
	ds_read_b128 v[244:247], v221 offset:40960
	v_add_f32_e32 v121, v94, v121
	v_add_f32_e32 v122, v118, v122
	v_add_f32_e32 v123, v231, v123
	v_add_f32_e32 v120, v87, v120
	v_add_f32_e32 v121, v95, v121
	v_add_f32_e32 v122, v119, v122
	v_add_f32_e32 v123, v249, v123
	s_waitcnt lgkmcnt(2)
	v_mfma_f32_32x32x16_bf16 v[96:111], v[162:165], v[150:153], v[96:111]
	v_mfma_f32_32x32x16_bf16 v[64:79], v[166:169], v[150:153], v[64:79]
	ds_read_b128 v[162:165], v222 offset:32768
	ds_read_b128 v[166:169], v222 offset:40960
	v_add_f32_e32 v120, v121, v120
	v_add_f32_e32 v121, v123, v122
	v_add_f32_e32 v229, v120, v121
	v_mov_b32_e32 v233, v229
	s_nop 1
	v_permlane32_swap_b32_e32 v229, v233
	v_cvt_pk_bf16_f32 v124, v80, v81
	v_cvt_pk_bf16_f32 v125, v82, v83
	v_cvt_pk_bf16_f32 v126, v84, v85
	s_waitcnt lgkmcnt(2)
	v_mfma_f32_32x32x16_bf16 v[96:111], v[240:243], v[146:149], v[96:111]
	v_mfma_f32_32x32x16_bf16 v[64:79], v[244:247], v[146:149], v[64:79]
	ds_read_b128 v[240:243], v224 offset:32768
	ds_read_b128 v[244:247], v224 offset:40960
	v_cvt_pk_bf16_f32 v127, v86, v87
	v_cvt_pk_bf16_f32 v120, v88, v89
	v_cvt_pk_bf16_f32 v121, v90, v91
	v_cvt_pk_bf16_f32 v122, v92, v93
	v_cvt_pk_bf16_f32 v123, v94, v95
	v_cvt_pk_bf16_f32 v112, v112, v113
	v_cvt_pk_bf16_f32 v113, v114, v115
	s_waitcnt lgkmcnt(2)
	v_mfma_f32_32x32x16_bf16 v[96:111], v[162:165], v[142:145], v[96:111]
	v_mfma_f32_32x32x16_bf16 v[64:79], v[166:169], v[142:145], v[64:79]
	ds_read_b128 v[162:165], v223 offset:32768
	ds_read_b128 v[166:169], v223 offset:40960
	v_cvt_pk_bf16_f32 v114, v116, v117
	v_cvt_pk_bf16_f32 v115, v118, v119
	v_cvt_pk_bf16_f32 v116, v234, v235
	v_cvt_pk_bf16_f32 v117, v236, v237
	v_cvt_pk_bf16_f32 v118, v238, v239
	v_cvt_pk_bf16_f32 v119, v231, v249
	s_waitcnt lgkmcnt(2)
	v_mfma_f32_32x32x16_bf16 v[96:111], v[240:243], v[134:137], v[96:111]
	v_mfma_f32_32x32x16_bf16 v[64:79], v[244:247], v[134:137], v[64:79]
	s_waitcnt lgkmcnt(0)
	v_mfma_f32_32x32x16_bf16 v[96:111], v[162:165], v[130:133], v[96:111]
	v_mfma_f32_32x32x16_bf16 v[64:79], v[166:169], v[130:133], v[64:79]
	s_min_i32 s2, s39, s14
	s_mul_i32 s2, s2, s62
	s_lshl_b32 s72, s2, 6
	s_lshl_b64 s[2:3], s[72:73], 1
	s_add_u32 s12, s10, s2
	s_addc_u32 s13, s11, s3
	s_add_u32 s2, s8, s2
	s_addc_u32 s3, s9, s3
	global_load_dwordx4 v[162:165], v128, s[12:13]
	global_load_dwordx4 v[166:169], v198, s[12:13]
	global_load_dwordx4 v[170:173], v128, s[2:3]
	global_load_dwordx4 v[174:177], v198, s[2:3]
	ds_read_b64_tr_b16 v[80:81], v211 offset:0
	ds_read_b64_tr_b16 v[82:83], v211 offset:0x800
	ds_read_b64_tr_b16 v[84:85], v211 offset:0x1000
	ds_read_b64_tr_b16 v[86:87], v211 offset:0x1800
	ds_read_b64_tr_b16 v[88:89], v211 offset:0x2000
	ds_read_b64_tr_b16 v[90:91], v211 offset:0x2800
	ds_read_b64_tr_b16 v[92:93], v211 offset:0x3000
	ds_read_b64_tr_b16 v[94:95], v211 offset:0x3800
	s_waitcnt lgkmcnt(0)
	s_nop 0
	v_mfma_f32_32x32x16_bf16 v[0:15], v[80:83], v[124:127], v[0:15]
	v_mfma_f32_32x32x16_bf16 v[0:15], v[84:87], v[120:123], v[0:15]
	v_mfma_f32_32x32x16_bf16 v[0:15], v[88:91], v[112:115], v[0:15]
	ds_read_b64_tr_b16 v[80:81], v211 offset:0x200
	ds_read_b64_tr_b16 v[82:83], v211 offset:0xa00
	ds_read_b64_tr_b16 v[84:85], v211 offset:0x1200
	v_mfma_f32_32x32x16_bf16 v[0:15], v[92:95], v[116:119], v[0:15]
	ds_read_b64_tr_b16 v[86:87], v211 offset:0x1a00
	ds_read_b64_tr_b16 v[88:89], v211 offset:0x2200
	ds_read_b64_tr_b16 v[90:91], v211 offset:0x2a00
	ds_read_b64_tr_b16 v[92:93], v211 offset:0x3200
	ds_read_b64_tr_b16 v[94:95], v211 offset:0x3a00
	s_waitcnt lgkmcnt(0)
	v_mfma_f32_32x32x16_bf16 v[48:63], v[80:83], v[124:127], v[48:63]
	v_mfma_f32_32x32x16_bf16 v[48:63], v[84:87], v[120:123], v[48:63]
	v_mfma_f32_32x32x16_bf16 v[48:63], v[88:91], v[112:115], v[48:63]
	ds_read_b64_tr_b16 v[80:81], v211 offset:0x400
	ds_read_b64_tr_b16 v[82:83], v211 offset:0xc00
	ds_read_b64_tr_b16 v[84:85], v211 offset:0x1400
	ds_read_b64_tr_b16 v[86:87], v211 offset:0x1c00
	v_mfma_f32_32x32x16_bf16 v[48:63], v[92:95], v[116:119], v[48:63]
	ds_read_b64_tr_b16 v[88:89], v211 offset:0x2400
	ds_read_b64_tr_b16 v[90:91], v211 offset:0x2c00
	ds_read_b64_tr_b16 v[92:93], v211 offset:0x3400
	ds_read_b64_tr_b16 v[94:95], v211 offset:0x3c00
	s_waitcnt lgkmcnt(0)
	v_mfma_f32_32x32x16_bf16 v[32:47], v[80:83], v[124:127], v[32:47]
	v_exp_f32_e32 v80, v64
	v_exp_f32_e32 v81, v65
	v_exp_f32_e32 v64, v96
	v_exp_f32_e32 v65, v97
	v_exp_f32_e32 v82, v66
	v_exp_f32_e32 v83, v67
	v_exp_f32_e32 v66, v98
	v_exp_f32_e32 v67, v99
	v_mfma_f32_32x32x16_bf16 v[32:47], v[84:87], v[120:123], v[32:47]
	v_exp_f32_e32 v84, v68
	v_exp_f32_e32 v85, v69
	v_exp_f32_e32 v68, v100
	v_exp_f32_e32 v69, v101
	v_exp_f32_e32 v86, v70
	v_exp_f32_e32 v87, v71
	v_exp_f32_e32 v70, v102
	v_exp_f32_e32 v71, v103
	v_mfma_f32_32x32x16_bf16 v[32:47], v[88:91], v[112:115], v[32:47]
	v_exp_f32_e32 v194, v72
	v_exp_f32_e32 v195, v73
	ds_read_b64_tr_b16 v[72:73], v211 offset:0x600
	v_exp_f32_e32 v196, v74
	v_exp_f32_e32 v197, v75
	ds_read_b64_tr_b16 v[74:75], v211 offset:0xe00
	v_mfma_f32_32x32x16_bf16 v[32:47], v[92:95], v[116:119], v[32:47]
	v_exp_f32_e32 v92, v76
	v_exp_f32_e32 v93, v77
	ds_read_b64_tr_b16 v[76:77], v211 offset:0x1600
	v_exp_f32_e32 v94, v78
	v_exp_f32_e32 v95, v79
	ds_read_b64_tr_b16 v[78:79], v211 offset:0x1e00
	ds_read_b64_tr_b16 v[96:97], v211 offset:0x2600
	ds_read_b64_tr_b16 v[98:99], v211 offset:0x2e00
	ds_read_b64_tr_b16 v[100:101], v211 offset:0x3600
	ds_read_b64_tr_b16 v[102:103], v211 offset:0x3e00
	s_waitcnt lgkmcnt(0)
	v_mfma_f32_32x32x16_bf16 v[16:31], v[72:75], v[124:127], v[16:31]
	v_exp_f32_e32 v72, v104
	v_exp_f32_e32 v73, v105
	v_exp_f32_e32 v74, v106
	v_exp_f32_e32 v75, v107
	v_mfma_f32_32x32x16_bf16 v[16:31], v[76:79], v[120:123], v[16:31]
	v_exp_f32_e32 v76, v108
	v_exp_f32_e32 v77, v109
	v_exp_f32_e32 v78, v110
	v_exp_f32_e32 v79, v111
	s_barrier
	v_mfma_f32_32x32x16_bf16 v[16:31], v[96:99], v[112:115], v[16:31]
	s_waitcnt vmcnt(4)
	s_waitcnt vmcnt(7)
	ds_write_b128 v212, v[178:181] offset:16384
	s_waitcnt vmcnt(6)
	ds_write_b128 v213, v[182:185] offset:16384
	s_waitcnt vmcnt(5)
	ds_write_b128 v214, v[186:189] offset:49152
	s_waitcnt vmcnt(4)
	ds_write_b128 v215, v[190:193] offset:49152
	v_mfma_f32_32x32x16_bf16 v[16:31], v[100:103], v[116:119], v[16:31]
